# c12
# speedup vs baseline: 1.0138x; 1.0003x over previous
.LBB2_8:
	s_or_b64 exec, exec, s[6:7]
	s_and_b32 s0, s2, 7
	s_lshr_b32 s40, s3, 3
	s_mul_i32 s42, s40, s0
	s_lshr_b32 s41, s2, 3
	s_add_i32 s42, s42, s41
	s_lshr_b32 s0, s42, 1
	v_mul_u32_u24_e32 v2, 0x156, v0
	v_lshrrev_b32_e32 v191, 5, v0
	s_and_b32 s33, s0, 28
	s_lshl_b32 s0, s42, 2
	v_lshrrev_b32_e32 v198, 16, v2
	s_and_b32 s3, s0, 28
	s_add_i32 s6, s33, -1
	v_mad_i32_i24 v2, v198, -6, v191
	v_add_u32_e32 v34, s6, v198
	v_add3_u32 v203, v2, s3, -1
	v_cmp_gt_u32_e32 vcc, 32, v34
	v_cmp_gt_u32_e64 s[0:1], 32, v203
	s_ashr_i32 s43, s42, 6
	v_and_b32_e32 v1, 31, v0
	s_and_b64 s[28:29], vcc, s[0:1]
	v_mov_b32_e32 v15, 0
	v_lshlrev_b32_e32 v30, 5, v34
	v_mov_b32_e32 v16, 0
	v_mov_b32_e32 v2, 0
	v_mov_b32_e32 v3, 0
	v_mov_b32_e32 v4, 0
	v_mov_b32_e32 v5, 0
	s_waitcnt lgkmcnt(0)
	s_nop 0
	s_and_saveexec_b64 s[0:1], s[28:29]
	s_cbranch_execz .LBB2_10
	s_lshl_b32 s4, s43, 10
	v_or3_b32 v2, v30, s4, v203
	v_lshl_or_b32 v6, v2, 10, v1
	v_ashrrev_i32_e32 v7, 31, v6
	v_lshl_add_u64 v[2:3], v[6:7], 4, s[12:13]
	v_lshl_add_u64 v[6:7], v[6:7], 2, s[14:15]
	global_load_dwordx4 v[2:5], v[2:3], off
	s_nop 0
	global_load_dword v16, v[6:7], off

.LBB6_445:
	s_or_b64 exec, exec, s[6:7]
	s_lshr_b32 s0, s56, 1
	s_and_b32 s40, s0, 28
	s_lshl_b32 s0, s22, 2
	v_mul_u32_u24_e32 v1, 0x156, v0
	s_and_b32 s41, s0, 28
	v_lshrrev_b32_e32 v195, 16, v1
	v_mul_i32_i24_e32 v196, -6, v195
	s_add_i32 s6, s40, -1
	s_add_i32 s4, s41, -1
	v_add_u32_e32 v34, s6, v195
	v_add3_u32 v1, s4, v191, v196
	v_cmp_gt_u32_e32 vcc, 32, v34
	v_cmp_gt_u32_e64 s[0:1], 32, v1
	s_lshr_b32 s42, s3, 6
	s_and_b64 s[28:29], vcc, s[0:1]
	v_mov_b32_e32 v14, 0
	v_lshlrev_b32_e32 v30, 5, v34
	v_mov_b32_e32 v15, 0
	v_mov_b32_e32 v2, 0
	v_mov_b32_e32 v3, 0
	v_mov_b32_e32 v4, 0
	v_mov_b32_e32 v5, 0
	s_waitcnt lgkmcnt(0)
	s_nop 0
	s_and_saveexec_b64 s[0:1], s[28:29]
	s_cbranch_execz .LBB6_447
	s_lshl_b32 s5, s42, 10
	v_or3_b32 v2, v30, s5, v1
	v_lshl_or_b32 v6, v2, 10, v206
	v_mov_b32_e32 v7, 0
	v_lshl_add_u64 v[2:3], v[6:7], 4, s[12:13]
	v_lshl_add_u64 v[6:7], v[6:7], 2, s[14:15]
	global_load_dwordx4 v[2:5], v[2:3], off
	s_nop 0
	global_load_dword v15, v[6:7], off
